# v89: M3 retention items: scanned states F/B requested behind Q, staged in registers and written to LDS (own barrier) after the score/PV loop; norm weights requested behind that barrier
# baseline (speedup 1.0000x reference)
.LBB0_555:
	s_and_b32 s33, s3, 1
	s_lshl_b32 s4, s33, 1
	s_add_i32 s14, s4, s18
	s_mul_i32 s4, s10, 0x1100
	s_lshl_b32 s5, s11, 7
	s_add_i32 s45, s4, s5
	s_lshl_b32 s22, s14, 6
	v_or_b32_e32 v2, s45, v116
	v_mov_b64_e32 v[50:51], s[88:89]
	s_mul_i32 s5, s14, 0x44
	s_ashr_i32 s23, s22, 31
	v_mad_i64_i32 v[2:3], s[14:15], v2, s60, v[50:51]
	s_lshl_b64 s[14:15], s[22:23], 1
	v_mov_b32_e32 v101, v0
	v_lshl_add_u64 v[2:3], v[2:3], 0, s[14:15]
	v_or_b32_e32 v10, s45, v117
	v_lshl_add_u64 v[2:3], v[2:3], 0, v[100:101]
	v_mad_i64_i32 v[10:11], s[26:27], v10, s60, v[50:51]
	s_mul_i32 s4, s10, 0x110
	v_add_co_u32_e32 v6, vcc, s78, v2
	v_lshl_add_u64 v[10:11], v[10:11], 0, s[14:15]
	v_or_b32_e32 v18, s45, v118
	s_add_i32 s4, s4, s5
	v_addc_co_u32_e32 v7, vcc, 0, v3, vcc
	v_lshl_add_u64 v[10:11], v[10:11], 0, v[100:101]
	v_mad_i64_i32 v[18:19], s[26:27], v18, s60, v[50:51]
	s_add_i32 s4, s4, s11
	v_add_co_u32_e32 v14, vcc, s78, v10
	v_lshl_add_u64 v[18:19], v[18:19], 0, s[14:15]
	v_or_b32_e32 v26, s45, v119
	s_ashr_i32 s5, s4, 31
	v_addc_co_u32_e32 v15, vcc, 0, v11, vcc
	v_lshl_add_u64 v[18:19], v[18:19], 0, v[100:101]
	v_mad_i64_i32 v[26:27], s[26:27], v26, s60, v[50:51]
	s_lshl_b64 s[10:11], s[4:5], 13
	s_add_i32 s4, s4, 34
	v_add_co_u32_e32 v22, vcc, s78, v18
	v_lshl_add_u64 v[26:27], v[26:27], 0, s[14:15]
	s_ashr_i32 s5, s4, 31
	v_addc_co_u32_e32 v23, vcc, 0, v19, vcc
	v_lshl_add_u64 v[26:27], v[26:27], 0, v[100:101]
	s_lshl_b64 s[4:5], s[4:5], 13
	v_add_co_u32_e32 v30, vcc, s78, v26
	s_cmp_eq_u32 s33, 0
	s_nop 0
	v_addc_co_u32_e32 v31, vcc, 0, v27, vcc
	s_cselect_b64 vcc, -1, 0
	s_add_u32 s10, s66, s10
	s_addc_u32 s11, s67, s11
	s_add_u32 s4, s66, s4
	s_addc_u32 s5, s67, s5
	v_or_b32_e32 v104, s45, v109
	global_load_dwordx4 v[2:5], v[6:7], off offset:512
	s_nop 0
	global_load_dwordx4 v[6:9], v[6:7], off
	s_nop 0
	global_load_dwordx4 v[10:13], v[14:15], off offset:512
	s_nop 0
	global_load_dwordx4 v[14:17], v[14:15], off
	s_nop 0
	global_load_dwordx4 v[18:21], v[22:23], off offset:512
	s_nop 0
	global_load_dwordx4 v[22:25], v[22:23], off
	s_nop 0
	global_load_dwordx4 v[26:29], v[30:31], off offset:512
	s_nop 0
	global_load_dwordx4 v[30:33], v[30:31], off
	s_nop 0
	v_mad_i64_i32 v[106:107], s[100:101], v104, s60, v[50:51]
	v_lshl_add_u64 v[50:51], v[106:107], 0, s[14:15]
	v_mov_b32_e32 v103, v0
	v_lshl_add_u64 v[50:51], v[50:51], 0, v[102:103]
	global_load_dwordx4 v[78:81], v[50:51], off offset:3584
	global_load_dwordx4 v[74:77], v[50:51], off offset:3616
	global_load_dwordx4 v[70:73], v[50:51], off offset:3648
	global_load_dwordx4 v[66:69], v[50:51], off offset:3680
	global_load_dwordx4 v[238:241], v125, s[10:11]
	global_load_dwordx4 v[242:245], v125, s[4:5]
	global_load_dwordx4 v[246:249], v126, s[10:11]
	global_load_dwordx4 v[250:253], v126, s[4:5]
	v_cndmask_b32_e32 v50, v142, v1, vcc
	s_mov_b32 s10, 0
	v_mul_f32_e32 v101, 0xbfb8aa3b, v50
	v_ashrrev_i32_e32 v105, 31, v104
	s_mov_b64 s[4:5], -1
	s_waitcnt vmcnt(15)
	ds_write_b128 v127, v[2:5]
	s_waitcnt vmcnt(14)
	ds_write_b128 v128, v[6:9] offset:16384
	s_waitcnt vmcnt(13)
	ds_write_b128 v129, v[10:13]
	s_waitcnt vmcnt(12)
	ds_write_b128 v130, v[14:17] offset:16384
	s_waitcnt vmcnt(11)
	ds_write_b128 v127, v[18:21] offset:8192
	s_waitcnt vmcnt(10)
	ds_write_b128 v131, v[22:25] offset:16384
	s_waitcnt vmcnt(9)
	ds_write_b128 v132, v[26:29] offset:8192
	s_waitcnt vmcnt(8)
	ds_write_b128 v133, v[30:33] offset:16384
	v_cndmask_b32_e32 v2, v143, v141, vcc
	v_mov_b32_e32 v18, 0
	v_mul_f32_e32 v103, 0xbfb8aa3b, v2
	v_mul_f32_e32 v167, 0xbf800000, v101
	v_mul_f32_e32 v168, 0xc0000000, v101
	v_mul_f32_e32 v169, 0xc0400000, v101
	v_mul_f32_e32 v170, 0xc1000000, v101
	v_mul_f32_e32 v171, 0x3f800000, v103
	v_mul_f32_e32 v172, 0x40000000, v103
	v_mul_f32_e32 v173, 0x40400000, v103
	v_mul_f32_e32 v174, 0x41000000, v103
	v_exp_f32_e32 v167, v167
	v_exp_f32_e32 v168, v168
	v_exp_f32_e32 v169, v169
	v_exp_f32_e32 v170, v170
	v_exp_f32_e32 v171, v171
	v_exp_f32_e32 v172, v172
	v_exp_f32_e32 v173, v173
	v_exp_f32_e32 v174, v174
	v_mov_b32_e32 v19, v18
	v_mov_b32_e32 v20, v18
	v_mov_b32_e32 v21, v18
	v_mov_b32_e32 v22, v18
	v_mov_b32_e32 v23, v18
	v_mov_b32_e32 v24, v18
	v_mov_b32_e32 v25, v18
	v_mov_b32_e32 v26, v18
	v_mov_b32_e32 v27, v18
	v_mov_b32_e32 v28, v18
	v_mov_b32_e32 v29, v18
	v_mov_b32_e32 v30, v18
	v_mov_b32_e32 v31, v18
	v_mov_b32_e32 v32, v18
	v_mov_b32_e32 v33, v18
	v_mov_b32_e32 v2, v18
	v_mov_b32_e32 v3, v18
	v_mov_b32_e32 v4, v18
	v_mov_b32_e32 v5, v18
	v_mov_b32_e32 v6, v18
	v_mov_b32_e32 v7, v18
	v_mov_b32_e32 v8, v18
	v_mov_b32_e32 v9, v18
	v_mov_b32_e32 v10, v18
	v_mov_b32_e32 v11, v18
	v_mov_b32_e32 v12, v18
	v_mov_b32_e32 v13, v18
	v_mov_b32_e32 v14, v18
	v_mov_b32_e32 v15, v18
	v_mov_b32_e32 v16, v18
	v_mov_b32_e32 v17, v18
	s_waitcnt lgkmcnt(0)
	s_barrier
	v_lshl_add_u64 v[152:153], s[22:23], 1, v[106:107]
	v_lshlrev_b32_e32 v154, 1, v82
	v_mov_b32_e32 v155, v0
	v_lshl_add_u64 v[152:153], v[152:153], 0, v[154:155]
	s_mov_b64 s[98:99], 0x1400
	v_lshl_add_u64 v[154:155], v[152:153], 0, s[98:99]
	v_add_co_u32_e32 v152, vcc, s78, v152
	v_addc_co_u32_e32 v153, vcc, 0, v153, vcc
	global_load_dwordx2 v[222:223], v[152:153], off offset:1024
	global_load_dwordx2 v[224:225], v[154:155], off offset:16
	global_load_dwordx2 v[226:227], v[154:155], off offset:32
	global_load_dwordx2 v[228:229], v[154:155], off offset:48
	global_load_dwordx2 v[230:231], v[154:155], off offset:64
	global_load_dwordx2 v[232:233], v[154:155], off offset:80
	global_load_dwordx2 v[234:235], v[154:155], off offset:96
	global_load_dwordx2 v[236:237], v[154:155], off offset:112
.LBB0_556:
	v_cndmask_b32_e64 v34, 0, 1, s[4:5]
	s_lshl_b32 s4, s10, 6
	v_cmp_ne_u32_e32 vcc, 1, v34
	v_or_b32_e32 v34, s4, v108
	v_lshl_add_u32 v152, v34, 7, s58
	v_add_u32_e32 v38, v152, v120
	ds_read_b128 v[34:37], v38 offset:16384
	ds_read_b128 v[50:53], v38 offset:20480
	v_add_u32_e32 v148, v152, v121
	s_waitcnt vmcnt(15) lgkmcnt(1)
	v_mfma_f32_32x32x16_bf16 v[34:49], v[34:37], v[78:81], 0
	ds_read_b128 v[144:147], v148 offset:16384
	ds_read_b128 v[148:151], v148 offset:20480
	s_waitcnt lgkmcnt(2)
	v_mfma_f32_32x32x16_bf16 v[50:65], v[50:53], v[78:81], 0
	s_waitcnt vmcnt(14) lgkmcnt(1)
	v_mfma_f32_32x32x16_bf16 v[34:49], v[144:147], v[74:77], v[34:49]
	s_waitcnt lgkmcnt(0)
	v_mfma_f32_32x32x16_bf16 v[50:65], v[148:151], v[74:77], v[50:65]
	v_add_u32_e32 v148, v152, v122
	ds_read_b128 v[144:147], v148 offset:16384
	ds_read_b128 v[148:151], v148 offset:20480
	s_waitcnt vmcnt(13) lgkmcnt(1)
	v_mfma_f32_32x32x16_bf16 v[34:49], v[144:147], v[70:73], v[34:49]
	s_waitcnt lgkmcnt(0)
	v_mfma_f32_32x32x16_bf16 v[50:65], v[148:151], v[70:73], v[50:65]
	v_add_u32_e32 v148, v152, v123
	ds_read_b128 v[144:147], v148 offset:16384
	ds_read_b128 v[148:151], v148 offset:20480
	s_waitcnt vmcnt(12) lgkmcnt(1)
	v_mfma_f32_32x32x16_bf16 v[34:49], v[144:147], v[66:69], v[34:49]
	v_or_b32_e32 v145, s4, v82
	s_waitcnt lgkmcnt(0)
	v_mfma_f32_32x32x16_bf16 v[50:65], v[148:151], v[66:69], v[50:65]
	v_sub_u32_e32 v166, v109, v145
	v_cvt_f32_i32_e32 v166, v166
	v_mul_f32_e32 v175, v101, v166
	v_mul_f32_e64 v183, -v103, v166
	v_exp_f32_e32 v175, v175
	v_exp_f32_e32 v183, v183
	s_nop 0
	v_mul_f32_e32 v176, v175, v170
	v_mul_f32_e32 v184, v183, v174
	v_mul_f32_e32 v177, v176, v170
	v_mul_f32_e32 v185, v184, v174
	v_mul_f32_e32 v178, v177, v170
	v_mul_f32_e32 v186, v185, v174
	v_mul_f32_e32 v179, v178, v170
	v_mul_f32_e32 v187, v186, v174
	v_mul_f32_e32 v180, v179, v170
	v_mul_f32_e32 v188, v187, v174
	v_mul_f32_e32 v181, v180, v170
	v_mul_f32_e32 v189, v188, v174
	v_mul_f32_e32 v182, v181, v170
	v_mul_f32_e32 v190, v189, v174
	v_min_f32_e32 v160, v175, v183
	v_mul_f32_e32 v144, v34, v160
	v_min_f32_e32 v162, v179, v187
	v_mul_f32_e32 v34, v50, v162
	v_mul_f32_e32 v164, v175, v167
	v_mul_f32_e32 v165, v183, v171
	v_min_f32_e32 v164, v164, v165
	v_mul_f32_e32 v50, v35, v164
	v_mul_f32_e32 v160, v179, v167
	v_mul_f32_e32 v161, v187, v171
	v_min_f32_e32 v160, v160, v161
	v_mul_f32_e32 v35, v51, v160
	v_mul_f32_e32 v162, v175, v168
	v_mul_f32_e32 v163, v183, v172
	v_min_f32_e32 v162, v162, v163
	v_mul_f32_e32 v51, v36, v162
	v_mul_f32_e32 v164, v179, v168
	v_mul_f32_e32 v165, v187, v172
	v_min_f32_e32 v164, v164, v165
	v_mul_f32_e32 v36, v52, v164
	v_mul_f32_e32 v160, v175, v169
	v_mul_f32_e32 v161, v183, v173
	v_min_f32_e32 v160, v160, v161
	v_mul_f32_e32 v52, v37, v160
	v_mul_f32_e32 v162, v179, v169
	v_mul_f32_e32 v163, v187, v173
	v_min_f32_e32 v162, v162, v163
	v_mul_f32_e32 v37, v53, v162
	v_min_f32_e32 v164, v176, v184
	v_mul_f32_e32 v53, v38, v164
	v_min_f32_e32 v160, v180, v188
	v_mul_f32_e32 v38, v54, v160
	v_mul_f32_e32 v162, v176, v167
	v_mul_f32_e32 v163, v184, v171
	v_min_f32_e32 v162, v162, v163
	v_mul_f32_e32 v54, v39, v162
	v_mul_f32_e32 v164, v180, v167
	v_mul_f32_e32 v165, v188, v171
	v_min_f32_e32 v164, v164, v165
	v_mul_f32_e32 v39, v55, v164
	v_mul_f32_e32 v160, v176, v168
	v_mul_f32_e32 v161, v184, v172
	v_min_f32_e32 v160, v160, v161
	v_mul_f32_e32 v55, v40, v160
	v_mul_f32_e32 v162, v180, v168
	v_mul_f32_e32 v163, v188, v172
	v_min_f32_e32 v162, v162, v163
	v_mul_f32_e32 v40, v56, v162
	v_mul_f32_e32 v164, v176, v169
	v_mul_f32_e32 v165, v184, v173
	v_min_f32_e32 v164, v164, v165
	v_mul_f32_e32 v56, v41, v164
	v_mul_f32_e32 v160, v180, v169
	v_mul_f32_e32 v161, v188, v173
	v_min_f32_e32 v160, v160, v161
	v_mul_f32_e32 v41, v57, v160
	v_min_f32_e32 v162, v177, v185
	v_mul_f32_e32 v57, v42, v162
	v_min_f32_e32 v164, v181, v189
	v_mul_f32_e32 v42, v58, v164
	v_mul_f32_e32 v160, v177, v167
	v_mul_f32_e32 v161, v185, v171
	v_min_f32_e32 v160, v160, v161
	v_mul_f32_e32 v43, v43, v160
	v_mul_f32_e32 v162, v181, v167
	v_mul_f32_e32 v163, v189, v171
	v_min_f32_e32 v162, v162, v163
	v_mul_f32_e32 v58, v59, v162
	v_mul_f32_e32 v164, v177, v168
	v_mul_f32_e32 v165, v185, v172
	v_min_f32_e32 v164, v164, v165
	v_mul_f32_e32 v59, v44, v164
	v_mul_f32_e32 v160, v181, v168
	v_mul_f32_e32 v161, v189, v172
	v_min_f32_e32 v160, v160, v161
	v_mul_f32_e32 v60, v60, v160
	v_mul_f32_e32 v162, v177, v169
	v_mul_f32_e32 v163, v185, v173
	v_min_f32_e32 v162, v162, v163
	v_mul_f32_e32 v147, v45, v162
	v_mul_f32_e32 v164, v181, v169
	v_mul_f32_e32 v165, v189, v173
	v_min_f32_e32 v164, v164, v165
	v_mul_f32_e32 v61, v61, v164
	v_min_f32_e32 v160, v178, v186
	v_mul_f32_e32 v146, v46, v160
	v_min_f32_e32 v162, v182, v190
	v_mul_f32_e32 v62, v62, v162
	v_mul_f32_e32 v164, v178, v167
	v_mul_f32_e32 v165, v186, v171
	v_min_f32_e32 v164, v164, v165
	v_mul_f32_e32 v148, v47, v164
	v_mul_f32_e32 v160, v182, v167
	v_mul_f32_e32 v161, v190, v171
	v_min_f32_e32 v160, v160, v161
	v_mul_f32_e32 v63, v63, v160
	v_mul_f32_e32 v162, v178, v168
	v_mul_f32_e32 v163, v186, v172
	v_min_f32_e32 v162, v162, v163
	v_mul_f32_e32 v149, v48, v162
	v_mul_f32_e32 v164, v182, v168
	v_mul_f32_e32 v165, v190, v172
	v_min_f32_e32 v164, v164, v165
	v_mul_f32_e32 v64, v64, v164
	v_mul_f32_e32 v160, v178, v169
	v_mul_f32_e32 v161, v186, v173
	v_min_f32_e32 v160, v160, v161
	v_mul_f32_e32 v145, v49, v160
	v_mul_f32_e32 v162, v182, v169
	v_mul_f32_e32 v163, v190, v173
	v_min_f32_e32 v162, v162, v163
	v_mul_f32_e32 v65, v65, v162
	v_cvt_pk_bf16_f32 v44, v144, v50
	v_cvt_pk_bf16_f32 v45, v51, v52
	v_cvt_pk_bf16_f32 v46, v53, v54
	v_cvt_pk_bf16_f32 v47, v55, v56
	v_cvt_pk_bf16_f32 v48, v57, v43
	v_cvt_pk_bf16_f32 v49, v59, v147
	v_cvt_pk_bf16_f32 v50, v146, v148
	v_cvt_pk_bf16_f32 v51, v149, v145
	v_cvt_pk_bf16_f32 v34, v34, v35
	v_cvt_pk_bf16_f32 v35, v36, v37
	v_cvt_pk_bf16_f32 v36, v38, v39
	v_cvt_pk_bf16_f32 v37, v40, v41
	v_cvt_pk_bf16_f32 v38, v42, v58
	v_cvt_pk_bf16_f32 v39, v60, v61
	v_cvt_pk_bf16_f32 v40, v62, v63
	v_cvt_pk_bf16_f32 v41, v64, v65
	v_lshl_add_u32 v42, s10, 13, v110
	ds_read_b64_tr_b16 v[52:53], v42 offset:0
	ds_read_b64_tr_b16 v[54:55], v42 offset:0x400
	ds_read_b64_tr_b16 v[56:57], v42 offset:0x800
	ds_read_b64_tr_b16 v[58:59], v42 offset:0xc00
	ds_read_b64_tr_b16 v[60:61], v42 offset:0x1000
	ds_read_b64_tr_b16 v[62:63], v42 offset:0x1400
	ds_read_b64_tr_b16 v[144:145], v42 offset:0x1800
	ds_read_b64_tr_b16 v[146:147], v42 offset:0x1c00
	s_waitcnt lgkmcnt(0)
	v_permlane32_swap_b32_e32 v44, v46
	v_permlane32_swap_b32_e32 v45, v47
	v_permlane32_swap_b32_e32 v48, v50
	v_permlane32_swap_b32_e32 v49, v51
	v_permlane32_swap_b32_e32 v34, v36
	v_permlane32_swap_b32_e32 v35, v37
	v_permlane32_swap_b32_e32 v38, v40
	v_permlane32_swap_b32_e32 v39, v41
	v_mfma_f32_32x32x16_bf16 v[18:33], v[52:55], v[44:47], v[18:33]
	ds_read_b64_tr_b16 v[52:53], v42 offset:0x200
	ds_read_b64_tr_b16 v[54:55], v42 offset:0x600
	v_mfma_f32_32x32x16_bf16 v[18:33], v[56:59], v[48:51], v[18:33]
	ds_read_b64_tr_b16 v[56:57], v42 offset:0xa00
	ds_read_b64_tr_b16 v[58:59], v42 offset:0xe00
	v_mfma_f32_32x32x16_bf16 v[18:33], v[60:63], v[34:37], v[18:33]
	ds_read_b64_tr_b16 v[60:61], v42 offset:0x1200
	ds_read_b64_tr_b16 v[62:63], v42 offset:0x1600
	v_mfma_f32_32x32x16_bf16 v[18:33], v[144:147], v[38:41], v[18:33]
	ds_read_b64_tr_b16 v[144:145], v42 offset:0x1a00
	ds_read_b64_tr_b16 v[146:147], v42 offset:0x1e00
	s_waitcnt lgkmcnt(0)
	v_mfma_f32_32x32x16_bf16 v[2:17], v[52:55], v[44:47], v[2:17]
	s_mov_b64 s[4:5], 0
	s_and_b64 vcc, exec, vcc
	s_mov_b32 s10, 1
	v_mfma_f32_32x32x16_bf16 v[2:17], v[56:59], v[48:51], v[2:17]
	v_mfma_f32_32x32x16_bf16 v[2:17], v[60:63], v[34:37], v[2:17]
	v_mfma_f32_32x32x16_bf16 v[2:17], v[144:147], v[38:41], v[2:17]
	s_cbranch_vccz .LBB0_556
	s_waitcnt vmcnt(11)
	ds_write_b128 v128, v[238:241] offset:32768
	s_waitcnt vmcnt(10)
	ds_write_b128 v128, v[242:245] offset:40960
	s_waitcnt vmcnt(9)
	ds_write_b128 v130, v[246:249] offset:32768
	s_waitcnt vmcnt(8)
	ds_write_b128 v130, v[250:253] offset:40960
	ds_read_b64 v[156:157], v0 offset:640
	s_lshl_b64 s[98:99], s[24:25], 2
	s_lshl_b64 s[100:101], s[22:23], 2
	s_waitcnt lgkmcnt(0)
	s_barrier
	s_add_u32 s98, s98, s100
	s_addc_u32 s99, s99, s101
	s_waitcnt lgkmcnt(0)
	v_readfirstlane_b32 s100, v156
	v_readfirstlane_b32 s101, v157
	v_lshlrev_b32_e32 v152, 2, v82
	s_add_u32 s98, s100, s98
	s_addc_u32 s99, s101, s99
	global_load_dwordx4 v[238:241], v152, s[98:99]
	global_load_dwordx4 v[242:245], v152, s[98:99] offset:32
	global_load_dwordx4 v[246:249], v152, s[98:99] offset:64
	global_load_dwordx4 v[250:253], v152, s[98:99] offset:96
	global_load_dwordx4 v[200:203], v152, s[98:99] offset:128
	global_load_dwordx4 v[204:207], v152, s[98:99] offset:160
	global_load_dwordx4 v[214:217], v152, s[98:99] offset:192
	global_load_dwordx4 v[192:195], v152, s[98:99] offset:224
	v_mul_f32_e32 v34, v101, v111
	v_exp_f32_e32 v50, v34
	v_mul_f32_e32 v34, v103, v112
	v_exp_f32_e32 v51, v34
	v_lshlrev_b32_e32 v35, 16, v78
	v_and_b32_e32 v36, 0xffff0000, v78
	v_mul_f32_e32 v34, v50, v35
	v_mul_f32_e32 v37, v50, v36
	v_mul_f32_e32 v36, v51, v36
	v_cvt_pk_bf16_f32 v34, v34, v37
	v_mul_f32_e32 v35, v51, v35
	v_cvt_pk_bf16_f32 v38, v35, v36
	v_lshlrev_b32_e32 v36, 16, v79
	v_and_b32_e32 v37, 0xffff0000, v79
	v_mul_f32_e32 v35, v50, v36
	v_mul_f32_e32 v39, v50, v37
	v_mul_f32_e32 v37, v51, v37
	v_cvt_pk_bf16_f32 v35, v35, v39
	v_mul_f32_e32 v36, v51, v36
	v_cvt_pk_bf16_f32 v39, v36, v37
	v_lshlrev_b32_e32 v37, 16, v80
	v_and_b32_e32 v40, 0xffff0000, v80
	v_mul_f32_e32 v36, v50, v37
	v_mul_f32_e32 v41, v50, v40
	v_cvt_pk_bf16_f32 v36, v36, v41
	v_mul_f32_e32 v37, v51, v37
	v_mul_f32_e32 v40, v51, v40
	v_lshlrev_b32_e32 v41, 16, v81
	v_and_b32_e32 v42, 0xffff0000, v81
	v_cvt_pk_bf16_f32 v40, v37, v40
	v_mul_f32_e32 v37, v50, v41
	v_mul_f32_e32 v43, v50, v42
	v_mul_f32_e32 v41, v51, v41
	v_mul_f32_e32 v42, v51, v42
	v_cvt_pk_bf16_f32 v37, v37, v43
	v_cvt_pk_bf16_f32 v41, v41, v42
	ds_read_b128 v[42:45], v134 offset:32768
	ds_read_b128 v[46:49], v134 offset:40960
	s_waitcnt lgkmcnt(1)
	v_mfma_f32_32x32x16_bf16 v[18:33], v[42:45], v[34:37], v[18:33]
	s_mov_b64 s[4:5], 0x1400
	s_waitcnt lgkmcnt(0)
	v_mfma_f32_32x32x16_bf16 v[18:33], v[46:49], v[38:41], v[18:33]
	ds_read_b128 v[42:45], v134 offset:36864
	ds_read_b128 v[46:49], v134 offset:45056
	s_waitcnt lgkmcnt(1)
	v_mfma_f32_32x32x16_bf16 v[2:17], v[42:45], v[34:37], v[2:17]
	v_lshlrev_b32_e32 v35, 16, v74
	v_and_b32_e32 v36, 0xffff0000, v74
	v_mul_f32_e32 v34, v50, v35
	v_mul_f32_e32 v37, v50, v36
	v_mul_f32_e32 v36, v51, v36
	v_cvt_pk_bf16_f32 v34, v34, v37
	v_mul_f32_e32 v35, v51, v35
	s_waitcnt lgkmcnt(0)
	v_mfma_f32_32x32x16_bf16 v[2:17], v[46:49], v[38:41], v[2:17]
	v_cvt_pk_bf16_f32 v38, v35, v36
	v_lshlrev_b32_e32 v36, 16, v75
	v_and_b32_e32 v37, 0xffff0000, v75
	v_mul_f32_e32 v35, v50, v36
	v_mul_f32_e32 v39, v50, v37
	v_mul_f32_e32 v37, v51, v37
	v_cvt_pk_bf16_f32 v35, v35, v39
	v_mul_f32_e32 v36, v51, v36
	v_cvt_pk_bf16_f32 v39, v36, v37
	v_lshlrev_b32_e32 v37, 16, v76
	v_and_b32_e32 v40, 0xffff0000, v76
	v_mul_f32_e32 v36, v50, v37
	v_mul_f32_e32 v41, v50, v40
	v_cvt_pk_bf16_f32 v36, v36, v41
	v_mul_f32_e32 v37, v51, v37
	v_mul_f32_e32 v40, v51, v40
	v_lshlrev_b32_e32 v41, 16, v77
	v_and_b32_e32 v42, 0xffff0000, v77
	v_cvt_pk_bf16_f32 v40, v37, v40
	v_mul_f32_e32 v37, v50, v41
	v_mul_f32_e32 v43, v50, v42
	v_mul_f32_e32 v41, v51, v41
	v_mul_f32_e32 v42, v51, v42
	v_cvt_pk_bf16_f32 v37, v37, v43
	v_cvt_pk_bf16_f32 v41, v41, v42
	ds_read_b128 v[42:45], v135 offset:32768
	ds_read_b128 v[46:49], v135 offset:40960
	s_waitcnt lgkmcnt(1)
	v_mfma_f32_32x32x16_bf16 v[18:33], v[42:45], v[34:37], v[18:33]
	s_waitcnt lgkmcnt(0)
	v_mfma_f32_32x32x16_bf16 v[18:33], v[46:49], v[38:41], v[18:33]
	ds_read_b128 v[42:45], v135 offset:36864
	ds_read_b128 v[46:49], v135 offset:45056
	s_waitcnt lgkmcnt(1)
	v_mfma_f32_32x32x16_bf16 v[2:17], v[42:45], v[34:37], v[2:17]
	v_lshlrev_b32_e32 v35, 16, v70
	v_and_b32_e32 v36, 0xffff0000, v70
	v_mul_f32_e32 v34, v50, v35
	v_mul_f32_e32 v37, v50, v36
	v_mul_f32_e32 v36, v51, v36
	v_cvt_pk_bf16_f32 v34, v34, v37
	v_mul_f32_e32 v35, v51, v35
	s_waitcnt lgkmcnt(0)
	v_mfma_f32_32x32x16_bf16 v[2:17], v[46:49], v[38:41], v[2:17]
	v_cvt_pk_bf16_f32 v38, v35, v36
	v_lshlrev_b32_e32 v36, 16, v71
	v_and_b32_e32 v37, 0xffff0000, v71
	v_mul_f32_e32 v35, v50, v36
	v_mul_f32_e32 v39, v50, v37
	v_mul_f32_e32 v37, v51, v37
	v_cvt_pk_bf16_f32 v35, v35, v39
	v_mul_f32_e32 v36, v51, v36
	v_cvt_pk_bf16_f32 v39, v36, v37
	v_lshlrev_b32_e32 v37, 16, v72
	v_and_b32_e32 v40, 0xffff0000, v72
	v_mul_f32_e32 v36, v50, v37
	v_mul_f32_e32 v41, v50, v40
	v_cvt_pk_bf16_f32 v36, v36, v41
	v_mul_f32_e32 v37, v51, v37
	v_mul_f32_e32 v40, v51, v40
	v_lshlrev_b32_e32 v41, 16, v73
	v_and_b32_e32 v42, 0xffff0000, v73
	v_cvt_pk_bf16_f32 v40, v37, v40
	v_mul_f32_e32 v37, v50, v41
	v_mul_f32_e32 v43, v50, v42
	v_mul_f32_e32 v41, v51, v41
	v_mul_f32_e32 v42, v51, v42
	v_cvt_pk_bf16_f32 v37, v37, v43
	v_cvt_pk_bf16_f32 v41, v41, v42
	ds_read_b128 v[42:45], v136 offset:32768
	ds_read_b128 v[46:49], v136 offset:40960
	s_waitcnt lgkmcnt(1)
	v_mfma_f32_32x32x16_bf16 v[18:33], v[42:45], v[34:37], v[18:33]
	s_waitcnt lgkmcnt(0)
	v_mfma_f32_32x32x16_bf16 v[18:33], v[46:49], v[38:41], v[18:33]
	ds_read_b128 v[42:45], v136 offset:36864
	ds_read_b128 v[46:49], v136 offset:45056
	s_waitcnt lgkmcnt(1)
	v_mfma_f32_32x32x16_bf16 v[2:17], v[42:45], v[34:37], v[2:17]
	v_lshlrev_b32_e32 v35, 16, v66
	v_and_b32_e32 v36, 0xffff0000, v66
	v_mul_f32_e32 v34, v50, v35
	v_mul_f32_e32 v37, v50, v36
	v_mul_f32_e32 v36, v51, v36
	v_cvt_pk_bf16_f32 v34, v34, v37
	v_mul_f32_e32 v35, v51, v35
	s_waitcnt lgkmcnt(0)
	v_mfma_f32_32x32x16_bf16 v[2:17], v[46:49], v[38:41], v[2:17]
	v_cvt_pk_bf16_f32 v38, v35, v36
	v_lshlrev_b32_e32 v36, 16, v67
	v_and_b32_e32 v37, 0xffff0000, v67
	v_mul_f32_e32 v35, v50, v36
	v_mul_f32_e32 v39, v50, v37
	v_mul_f32_e32 v37, v51, v37
	v_cvt_pk_bf16_f32 v35, v35, v39
	v_mul_f32_e32 v36, v51, v36
	v_cvt_pk_bf16_f32 v39, v36, v37
	v_lshlrev_b32_e32 v37, 16, v68
	v_and_b32_e32 v40, 0xffff0000, v68
	v_mul_f32_e32 v36, v50, v37
	v_mul_f32_e32 v41, v50, v40
	v_cvt_pk_bf16_f32 v36, v36, v41
	v_mul_f32_e32 v37, v51, v37
	v_mul_f32_e32 v40, v51, v40
	v_lshlrev_b32_e32 v41, 16, v69
	v_and_b32_e32 v42, 0xffff0000, v69
	v_cvt_pk_bf16_f32 v40, v37, v40
	v_mul_f32_e32 v37, v50, v41
	v_mul_f32_e32 v43, v50, v42
	v_mul_f32_e32 v41, v51, v41
	v_mul_f32_e32 v42, v51, v42
	v_cvt_pk_bf16_f32 v37, v37, v43
	v_cvt_pk_bf16_f32 v41, v41, v42
	ds_read_b128 v[42:45], v137 offset:32768
	ds_read_b128 v[46:49], v137 offset:40960
	s_waitcnt lgkmcnt(1)
	v_mfma_f32_32x32x16_bf16 v[18:33], v[42:45], v[34:37], v[18:33]
	s_waitcnt lgkmcnt(0)
	v_mfma_f32_32x32x16_bf16 v[18:33], v[46:49], v[38:41], v[18:33]
	ds_read_b128 v[42:45], v137 offset:36864
	ds_read_b128 v[46:49], v137 offset:45056
	s_waitcnt lgkmcnt(1)
	v_mfma_f32_32x32x16_bf16 v[2:17], v[42:45], v[34:37], v[2:17]
	s_waitcnt lgkmcnt(0)
	v_mfma_f32_32x32x16_bf16 v[2:17], v[46:49], v[38:41], v[2:17]
	s_nop 7
	v_mul_f32_e32 v78, v19, v19
	v_fmac_f32_e32 v78, v18, v18
	v_fmac_f32_e32 v78, v20, v20
	v_fmac_f32_e32 v78, v21, v21
	v_fmac_f32_e32 v78, v22, v22
	v_fmac_f32_e32 v78, v23, v23
	v_fmac_f32_e32 v78, v24, v24
	v_fmac_f32_e32 v78, v25, v25
	v_fmac_f32_e32 v78, v26, v26
	v_fmac_f32_e32 v78, v27, v27
	v_fmac_f32_e32 v78, v28, v28
	v_fmac_f32_e32 v78, v29, v29
	v_fmac_f32_e32 v78, v30, v30
	v_fmac_f32_e32 v78, v31, v31
	v_fmac_f32_e32 v78, v32, v32
	v_fmac_f32_e32 v78, v33, v33
	v_fmac_f32_e32 v78, v2, v2
	v_fmac_f32_e32 v78, v3, v3
	v_fmac_f32_e32 v78, v4, v4
	v_fmac_f32_e32 v78, v5, v5
	v_fmac_f32_e32 v78, v6, v6
	v_fmac_f32_e32 v78, v7, v7
	v_fmac_f32_e32 v78, v8, v8
	v_fmac_f32_e32 v78, v9, v9
	v_fmac_f32_e32 v78, v10, v10
	v_fmac_f32_e32 v78, v11, v11
	v_fmac_f32_e32 v78, v12, v12
	v_fmac_f32_e32 v78, v13, v13
	v_fmac_f32_e32 v78, v14, v14
	v_fmac_f32_e32 v78, v15, v15
	v_pk_mul_f32 v[62:63], v[16:17], v[16:17]
	s_and_b64 vcc, exec, s[20:21]
	v_add_f32_e32 v62, v78, v62
	v_add_f32_e32 v62, v62, v63
	v_mov_b32_e32 v63, v62
	s_nop 1
	v_permlane32_swap_b32_e32 v62, v63
	v_add_f32_e32 v62, v62, v63
	v_fmamk_f32 v62, v62, 0x3c800000, v210
	v_rsq_f32_e32 v78, v62
	v_lshlrev_b64 v[62:63], 10, v[104:105]
	v_lshl_add_u64 v[62:63], s[82:83], 0, v[62:63]
	v_lshl_add_u64 v[62:63], v[62:63], 0, s[22:23]
	v_mul_f32_e32 v78, 0x41800000, v78
	v_lshl_add_u64 v[62:63], v[62:63], 0, v[84:85]
	v_rcp_f32_e32 v152, v78
	s_waitcnt vmcnt(7)
	v_lshlrev_b32_e32 v153, 16, v222
	v_and_b32_e32 v154, 0xffff0000, v222
	v_lshlrev_b32_e32 v155, 16, v223
	v_and_b32_e32 v156, 0xffff0000, v223
	v_mul_f32_e32 v157, 0xbfb8aa3b, v153
	v_mul_f32_e32 v158, 0xbfb8aa3b, v154
	v_mul_f32_e32 v159, 0xbfb8aa3b, v155
	v_mul_f32_e32 v160, 0xbfb8aa3b, v156
	v_exp_f32_e32 v157, v157
	v_exp_f32_e32 v158, v158
	v_exp_f32_e32 v159, v159
	v_exp_f32_e32 v160, v160
	v_mul_f32_e32 v161, v18, v238
	v_mul_f32_e32 v162, v19, v239
	v_mul_f32_e32 v163, v20, v240
	v_mul_f32_e32 v164, v21, v241
	v_fma_f32 v157, v157, v152, v152
	v_fma_f32 v158, v158, v152, v152
	v_fma_f32 v159, v159, v152, v152
	v_fma_f32 v160, v160, v152, v152
	v_rcp_f32_e32 v157, v157
	v_rcp_f32_e32 v158, v158
	v_rcp_f32_e32 v159, v159
	v_rcp_f32_e32 v160, v160
	v_mul_f32_e32 v153, v153, v157
	v_mul_f32_e32 v154, v154, v158
	v_mul_f32_e32 v155, v155, v159
	v_mul_f32_e32 v156, v156, v160
	v_mul_f32_e32 v161, v161, v153
	v_mul_f32_e32 v162, v162, v154
	v_mul_f32_e32 v163, v163, v155
	v_mul_f32_e32 v164, v164, v156
	v_cvt_pk_fp8_f32 v18, v161, v162
	v_cvt_pk_fp8_f32 v18, v163, v164 op_sel:[0,0,1]
	s_waitcnt vmcnt(6)
	v_lshlrev_b32_e32 v165, 16, v224
	v_and_b32_e32 v166, 0xffff0000, v224
	v_lshlrev_b32_e32 v167, 16, v225
	v_and_b32_e32 v168, 0xffff0000, v225
	v_mul_f32_e32 v169, 0xbfb8aa3b, v165
	v_mul_f32_e32 v170, 0xbfb8aa3b, v166
	v_mul_f32_e32 v171, 0xbfb8aa3b, v167
	v_mul_f32_e32 v172, 0xbfb8aa3b, v168
	v_exp_f32_e32 v169, v169
	v_exp_f32_e32 v170, v170
	v_exp_f32_e32 v171, v171
	v_exp_f32_e32 v172, v172
	v_mul_f32_e32 v173, v22, v242
	v_mul_f32_e32 v174, v23, v243
	v_mul_f32_e32 v175, v24, v244
	v_mul_f32_e32 v176, v25, v245
	v_fma_f32 v169, v169, v152, v152
	v_fma_f32 v170, v170, v152, v152
	v_fma_f32 v171, v171, v152, v152
	v_fma_f32 v172, v172, v152, v152
	v_rcp_f32_e32 v169, v169
	v_rcp_f32_e32 v170, v170
	v_rcp_f32_e32 v171, v171
	v_rcp_f32_e32 v172, v172
	v_mul_f32_e32 v165, v165, v169
	v_mul_f32_e32 v166, v166, v170
	v_mul_f32_e32 v167, v167, v171
	v_mul_f32_e32 v168, v168, v172
	v_mul_f32_e32 v173, v173, v165
	v_mul_f32_e32 v174, v174, v166
	v_mul_f32_e32 v175, v175, v167
	v_mul_f32_e32 v176, v176, v168
	v_cvt_pk_fp8_f32 v20, v173, v174
	v_cvt_pk_fp8_f32 v20, v175, v176 op_sel:[0,0,1]
	s_waitcnt vmcnt(5)
	v_lshlrev_b32_e32 v153, 16, v226
	v_and_b32_e32 v154, 0xffff0000, v226
	v_lshlrev_b32_e32 v155, 16, v227
	v_and_b32_e32 v156, 0xffff0000, v227
	v_mul_f32_e32 v157, 0xbfb8aa3b, v153
	v_mul_f32_e32 v158, 0xbfb8aa3b, v154
	v_mul_f32_e32 v159, 0xbfb8aa3b, v155
	v_mul_f32_e32 v160, 0xbfb8aa3b, v156
	v_exp_f32_e32 v157, v157
	v_exp_f32_e32 v158, v158
	v_exp_f32_e32 v159, v159
	v_exp_f32_e32 v160, v160
	v_mul_f32_e32 v161, v26, v246
	v_mul_f32_e32 v162, v27, v247
	v_mul_f32_e32 v163, v28, v248
	v_mul_f32_e32 v164, v29, v249
	v_fma_f32 v157, v157, v152, v152
	v_fma_f32 v158, v158, v152, v152
	v_fma_f32 v159, v159, v152, v152
	v_fma_f32 v160, v160, v152, v152
	v_rcp_f32_e32 v157, v157
	v_rcp_f32_e32 v158, v158
	v_rcp_f32_e32 v159, v159
	v_rcp_f32_e32 v160, v160
	v_mul_f32_e32 v153, v153, v157
	v_mul_f32_e32 v154, v154, v158
	v_mul_f32_e32 v155, v155, v159
	v_mul_f32_e32 v156, v156, v160
	v_mul_f32_e32 v161, v161, v153
	v_mul_f32_e32 v162, v162, v154
	v_mul_f32_e32 v163, v163, v155
	v_mul_f32_e32 v164, v164, v156
	v_cvt_pk_fp8_f32 v19, v161, v162
	v_cvt_pk_fp8_f32 v19, v163, v164 op_sel:[0,0,1]
	s_waitcnt vmcnt(4)
	v_lshlrev_b32_e32 v165, 16, v228
	v_and_b32_e32 v166, 0xffff0000, v228
	v_lshlrev_b32_e32 v167, 16, v229
	v_and_b32_e32 v168, 0xffff0000, v229
	v_mul_f32_e32 v169, 0xbfb8aa3b, v165
	v_mul_f32_e32 v170, 0xbfb8aa3b, v166
	v_mul_f32_e32 v171, 0xbfb8aa3b, v167
	v_mul_f32_e32 v172, 0xbfb8aa3b, v168
	v_exp_f32_e32 v169, v169
	v_exp_f32_e32 v170, v170
	v_exp_f32_e32 v171, v171
	v_exp_f32_e32 v172, v172
	v_mul_f32_e32 v173, v30, v250
	v_mul_f32_e32 v174, v31, v251
	v_mul_f32_e32 v175, v32, v252
	v_mul_f32_e32 v176, v33, v253
	v_fma_f32 v169, v169, v152, v152
	v_fma_f32 v170, v170, v152, v152
	v_fma_f32 v171, v171, v152, v152
	v_fma_f32 v172, v172, v152, v152
	v_rcp_f32_e32 v169, v169
	v_rcp_f32_e32 v170, v170
	v_rcp_f32_e32 v171, v171
	v_rcp_f32_e32 v172, v172
	v_mul_f32_e32 v165, v165, v169
	v_mul_f32_e32 v166, v166, v170
	v_mul_f32_e32 v167, v167, v171
	v_mul_f32_e32 v168, v168, v172
	v_mul_f32_e32 v173, v173, v165
	v_mul_f32_e32 v174, v174, v166
	v_mul_f32_e32 v175, v175, v167
	v_mul_f32_e32 v176, v176, v168
	v_cvt_pk_fp8_f32 v21, v173, v174
	v_cvt_pk_fp8_f32 v21, v175, v176 op_sel:[0,0,1]
	v_permlane32_swap_b32_e32 v18, v19
	s_nop 0
	v_permlane32_swap_b32_e32 v20, v21
	global_store_dwordx4 v[62:63], v[18:21], off offset:768
	s_waitcnt vmcnt(4)
	v_lshlrev_b32_e32 v153, 16, v230
	v_and_b32_e32 v154, 0xffff0000, v230
	v_lshlrev_b32_e32 v155, 16, v231
	v_and_b32_e32 v156, 0xffff0000, v231
	v_mul_f32_e32 v157, 0xbfb8aa3b, v153
	v_mul_f32_e32 v158, 0xbfb8aa3b, v154
	v_mul_f32_e32 v159, 0xbfb8aa3b, v155
	v_mul_f32_e32 v160, 0xbfb8aa3b, v156
	v_exp_f32_e32 v157, v157
	v_exp_f32_e32 v158, v158
	v_exp_f32_e32 v159, v159
	v_exp_f32_e32 v160, v160
	v_mul_f32_e32 v161, v2, v200
	v_mul_f32_e32 v162, v3, v201
	v_mul_f32_e32 v163, v4, v202
	v_mul_f32_e32 v164, v5, v203
	v_fma_f32 v157, v157, v152, v152
	v_fma_f32 v158, v158, v152, v152
	v_fma_f32 v159, v159, v152, v152
	v_fma_f32 v160, v160, v152, v152
	v_rcp_f32_e32 v157, v157
	v_rcp_f32_e32 v158, v158
	v_rcp_f32_e32 v159, v159
	v_rcp_f32_e32 v160, v160
	v_mul_f32_e32 v153, v153, v157
	v_mul_f32_e32 v154, v154, v158
	v_mul_f32_e32 v155, v155, v159
	v_mul_f32_e32 v156, v156, v160
	v_mul_f32_e32 v161, v161, v153
	v_mul_f32_e32 v162, v162, v154
	v_mul_f32_e32 v163, v163, v155
	v_mul_f32_e32 v164, v164, v156
	v_cvt_pk_fp8_f32 v2, v161, v162
	v_cvt_pk_fp8_f32 v2, v163, v164 op_sel:[0,0,1]
	s_waitcnt vmcnt(3)
	v_lshlrev_b32_e32 v165, 16, v232
	v_and_b32_e32 v166, 0xffff0000, v232
	v_lshlrev_b32_e32 v167, 16, v233
	v_and_b32_e32 v168, 0xffff0000, v233
	v_mul_f32_e32 v169, 0xbfb8aa3b, v165
	v_mul_f32_e32 v170, 0xbfb8aa3b, v166
	v_mul_f32_e32 v171, 0xbfb8aa3b, v167
	v_mul_f32_e32 v172, 0xbfb8aa3b, v168
	v_exp_f32_e32 v169, v169
	v_exp_f32_e32 v170, v170
	v_exp_f32_e32 v171, v171
	v_exp_f32_e32 v172, v172
	v_mul_f32_e32 v173, v6, v204
	v_mul_f32_e32 v174, v7, v205
	v_mul_f32_e32 v175, v8, v206
	v_mul_f32_e32 v176, v9, v207
	v_fma_f32 v169, v169, v152, v152
	v_fma_f32 v170, v170, v152, v152
	v_fma_f32 v171, v171, v152, v152
	v_fma_f32 v172, v172, v152, v152
	v_rcp_f32_e32 v169, v169
	v_rcp_f32_e32 v170, v170
	v_rcp_f32_e32 v171, v171
	v_rcp_f32_e32 v172, v172
	v_mul_f32_e32 v165, v165, v169
	v_mul_f32_e32 v166, v166, v170
	v_mul_f32_e32 v167, v167, v171
	v_mul_f32_e32 v168, v168, v172
	v_mul_f32_e32 v173, v173, v165
	v_mul_f32_e32 v174, v174, v166
	v_mul_f32_e32 v175, v175, v167
	v_mul_f32_e32 v176, v176, v168
	v_cvt_pk_fp8_f32 v4, v173, v174
	v_cvt_pk_fp8_f32 v4, v175, v176 op_sel:[0,0,1]
	s_waitcnt vmcnt(2)
	v_lshlrev_b32_e32 v153, 16, v234
	v_and_b32_e32 v154, 0xffff0000, v234
	v_lshlrev_b32_e32 v155, 16, v235
	v_and_b32_e32 v156, 0xffff0000, v235
	v_mul_f32_e32 v157, 0xbfb8aa3b, v153
	v_mul_f32_e32 v158, 0xbfb8aa3b, v154
	v_mul_f32_e32 v159, 0xbfb8aa3b, v155
	v_mul_f32_e32 v160, 0xbfb8aa3b, v156
	v_exp_f32_e32 v157, v157
	v_exp_f32_e32 v158, v158
	v_exp_f32_e32 v159, v159
	v_exp_f32_e32 v160, v160
	v_mul_f32_e32 v161, v10, v214
	v_mul_f32_e32 v162, v11, v215
	v_mul_f32_e32 v163, v12, v216
	v_mul_f32_e32 v164, v13, v217
	v_fma_f32 v157, v157, v152, v152
	v_fma_f32 v158, v158, v152, v152
	v_fma_f32 v159, v159, v152, v152
	v_fma_f32 v160, v160, v152, v152
	v_rcp_f32_e32 v157, v157
	v_rcp_f32_e32 v158, v158
	v_rcp_f32_e32 v159, v159
	v_rcp_f32_e32 v160, v160
	v_mul_f32_e32 v153, v153, v157
	v_mul_f32_e32 v154, v154, v158
	v_mul_f32_e32 v155, v155, v159
	v_mul_f32_e32 v156, v156, v160
	v_mul_f32_e32 v161, v161, v153
	v_mul_f32_e32 v162, v162, v154
	v_mul_f32_e32 v163, v163, v155
	v_mul_f32_e32 v164, v164, v156
	v_cvt_pk_fp8_f32 v3, v161, v162
	v_cvt_pk_fp8_f32 v3, v163, v164 op_sel:[0,0,1]
	s_waitcnt vmcnt(1)
	v_lshlrev_b32_e32 v165, 16, v236
	v_and_b32_e32 v166, 0xffff0000, v236
	v_lshlrev_b32_e32 v167, 16, v237
	v_and_b32_e32 v168, 0xffff0000, v237
	v_mul_f32_e32 v169, 0xbfb8aa3b, v165
	v_mul_f32_e32 v170, 0xbfb8aa3b, v166
	v_mul_f32_e32 v171, 0xbfb8aa3b, v167
	v_mul_f32_e32 v172, 0xbfb8aa3b, v168
	v_exp_f32_e32 v169, v169
	v_exp_f32_e32 v170, v170
	v_exp_f32_e32 v171, v171
	v_exp_f32_e32 v172, v172
	v_mul_f32_e32 v173, v14, v192
	v_mul_f32_e32 v174, v15, v193
	v_mul_f32_e32 v175, v16, v194
	v_mul_f32_e32 v176, v17, v195
	v_fma_f32 v169, v169, v152, v152
	v_fma_f32 v170, v170, v152, v152
	v_fma_f32 v171, v171, v152, v152
	v_fma_f32 v172, v172, v152, v152
	v_rcp_f32_e32 v169, v169
	v_rcp_f32_e32 v170, v170
	v_rcp_f32_e32 v171, v171
	v_rcp_f32_e32 v172, v172
	v_mul_f32_e32 v165, v165, v169
	v_mul_f32_e32 v166, v166, v170
	v_mul_f32_e32 v167, v167, v171
	v_mul_f32_e32 v168, v168, v172
	v_mul_f32_e32 v173, v173, v165
	v_mul_f32_e32 v174, v174, v166
	v_mul_f32_e32 v175, v175, v167
	v_mul_f32_e32 v176, v176, v168
	v_cvt_pk_fp8_f32 v5, v173, v174
	v_cvt_pk_fp8_f32 v5, v175, v176 op_sel:[0,0,1]
	v_permlane32_swap_b32_e32 v2, v3
	s_nop 0
	v_permlane32_swap_b32_e32 v4, v5
	global_store_dwordx4 v[62:63], v[2:5], off offset:800
	s_cbranch_vccz .LBB0_550
	s_waitcnt vmcnt(0)
	s_barrier
	s_and_saveexec_b64 s[4:5], s[0:1]
	s_cbranch_execz .LBB0_549
	s_mov_b64 s[10:11], exec
	v_mbcnt_lo_u32_b32 v2, s10, 0
	buffer_wbl2 sc1
	s_waitcnt vmcnt(0)
	s_waitcnt vmcnt(0)
	v_mbcnt_hi_u32_b32 v2, s11, v2
	v_cmp_eq_u32_e32 vcc, 0, v2
	s_and_b64 s[14:15], exec, vcc
	s_mov_b64 exec, s[14:15]
	s_cbranch_execz .LBB0_549
	s_bcnt1_i32_b64 s10, s[10:11]
	v_mov_b32_e32 v2, s10
	global_atomic_add v0, v2, s[84:85]
	s_branch .LBB0_549
